# QK^T fragment read pipelining also in the MoBA and DSA attention loop bodies (registers found dead by a def-use scan)
# speedup vs baseline: 1.0188x; 1.0004x over previous
.LBB0_1143:
	v_add_u32_e32 v66, 64, v216
	v_cvt_f32_i32_e32 v67, v66
	s_waitcnt vmcnt(0)
	v_lshrrev_b32_e32 v83, v208, v196
	v_and_b32_e32 v66, 1, v83
	v_cmp_eq_u32_e32 vcc, 1, v66
	v_mul_f32_e64 v82, -v178, v67
	v_fma_f32 v68, 0, v178, v82
	v_cndmask_b32_e32 v66, v243, v68, vcc
	v_and_b32_e32 v68, 2, v83
	v_fma_f32 v67, -v178, v67, v178
	v_cmp_ne_u32_e32 vcc, 0, v68
	v_and_b32_e32 v70, 8, v83
	v_pk_fma_f32 v[68:69], v[188:189], s[60:61], v[82:83] op_sel_hi:[1,1,0]
	v_cndmask_b32_e32 v67, v243, v67, vcc
	v_and_b32_e32 v71, 4, v83
	v_cmp_ne_u32_e32 vcc, 0, v70
	v_and_b32_e32 v72, 0x200, v83
	v_and_b32_e32 v73, 0x100, v83
	v_cndmask_b32_e32 v69, v243, v69, vcc
	v_cmp_ne_u32_e32 vcc, 0, v71
	v_pk_fma_f32 v[70:71], v[188:189], s[74:75], v[82:83] op_sel_hi:[1,1,0]
	v_and_b32_e32 v74, 0x800, v83
	v_cndmask_b32_e32 v68, v243, v68, vcc
	v_cmp_ne_u32_e32 vcc, 0, v72
	v_and_b32_e32 v75, 0x400, v83
	v_and_b32_e32 v76, 0x20000, v83
	v_cndmask_b32_e32 v71, v243, v71, vcc
	v_cmp_ne_u32_e32 vcc, 0, v73
	v_pk_fma_f32 v[72:73], v[188:189], s[62:63], v[82:83] op_sel_hi:[1,1,0]
	v_and_b32_e32 v77, 0x10000, v83
	v_cndmask_b32_e32 v70, v243, v70, vcc
	v_cmp_ne_u32_e32 vcc, 0, v74
	s_mov_b32 s2, 0x41900000
	s_mov_b32 s3, 0x41980000
	v_cndmask_b32_e32 v73, v243, v73, vcc
	v_cmp_ne_u32_e32 vcc, 0, v75
	v_pk_fma_f32 v[74:75], v[188:189], s[58:59], v[82:83] op_sel_hi:[1,1,0]
	v_and_b32_e32 v78, 0x80000, v83
	v_cndmask_b32_e32 v72, v243, v72, vcc
	v_cmp_ne_u32_e32 vcc, 0, v76
	v_and_b32_e32 v79, 0x40000, v83
	v_and_b32_e32 v80, 0x2000000, v83
	v_cndmask_b32_e32 v75, v243, v75, vcc
	v_cmp_ne_u32_e32 vcc, 0, v77
	v_pk_fma_f32 v[76:77], v[188:189], s[2:3], v[82:83] op_sel_hi:[1,1,0]
	s_mov_b32 s2, 0x41c00000
	v_cndmask_b32_e32 v74, v243, v74, vcc
	v_cmp_ne_u32_e32 vcc, 0, v78
	s_mov_b32 s3, 0x41c80000
	v_and_b32_e32 v81, 0x1000000, v83
	v_cndmask_b32_e32 v77, v243, v77, vcc
	v_cmp_ne_u32_e32 vcc, 0, v79
	v_pk_fma_f32 v[78:79], v[188:189], s[2:3], v[82:83] op_sel_hi:[1,1,0]
	s_mov_b32 s2, 0x41d00000
	v_cndmask_b32_e32 v76, v243, v76, vcc
	v_cmp_ne_u32_e32 vcc, 0, v80
	s_mov_b32 s3, 0x41d80000
	v_and_b32_e32 v84, 0x8000000, v83
	v_cndmask_b32_e32 v79, v243, v79, vcc
	v_cmp_ne_u32_e32 vcc, 0, v81
	v_lshrrev_b32_e32 v98, v208, v197
	v_pk_fma_f32 v[80:81], v[188:189], s[2:3], v[82:83] op_sel_hi:[1,1,0]
	v_cndmask_b32_e32 v78, v243, v78, vcc
	v_and_b32_e32 v83, 0x4000000, v83
	v_cmp_ne_u32_e32 vcc, 0, v84
	v_and_b32_e32 v99, 0x8000000, v98
	v_pk_fma_f32 v[96:97], v[188:189], s[68:69], v[82:83] op_sel_hi:[1,1,0]
	v_cndmask_b32_e32 v81, v243, v81, vcc
	v_cmp_ne_u32_e32 vcc, 0, v83
	v_pk_fma_f32 v[94:95], v[188:189], s[96:97], v[82:83] op_sel_hi:[1,1,0]
	v_pk_fma_f32 v[92:93], v[188:189], s[94:95], v[82:83] op_sel_hi:[1,1,0]
	v_cndmask_b32_e32 v80, v243, v80, vcc
	v_cmp_ne_u32_e32 vcc, 0, v99
	v_and_b32_e32 v99, 0x4000000, v98
	v_pk_fma_f32 v[90:91], v[188:189], s[92:93], v[82:83] op_sel_hi:[1,1,0]
	v_cndmask_b32_e32 v97, v243, v97, vcc
	v_cmp_ne_u32_e32 vcc, 0, v99
	v_and_b32_e32 v99, 0x2000000, v98
	v_pk_fma_f32 v[88:89], v[188:189], s[90:91], v[82:83] op_sel_hi:[1,1,0]
	v_cndmask_b32_e32 v96, v243, v96, vcc
	v_cmp_ne_u32_e32 vcc, 0, v99
	v_and_b32_e32 v99, 0x1000000, v98
	v_pk_fma_f32 v[86:87], v[188:189], s[88:89], v[82:83] op_sel_hi:[1,1,0]
	v_cndmask_b32_e32 v95, v243, v95, vcc
	v_cmp_ne_u32_e32 vcc, 0, v99
	v_and_b32_e32 v99, 0x80000, v98
	v_pk_fma_f32 v[84:85], v[188:189], s[86:87], v[82:83] op_sel_hi:[1,1,0]
	v_cndmask_b32_e32 v94, v243, v94, vcc
	v_cmp_ne_u32_e32 vcc, 0, v99
	v_and_b32_e32 v99, 0x40000, v98
	s_mov_b32 s2, 0x42000000
	v_cndmask_b32_e32 v93, v243, v93, vcc
	v_cmp_ne_u32_e32 vcc, 0, v99
	v_and_b32_e32 v99, 0x20000, v98
	s_mov_b32 s3, 0x42040000
	v_cndmask_b32_e32 v92, v243, v92, vcc
	v_cmp_ne_u32_e32 vcc, 0, v99
	v_and_b32_e32 v99, 0x10000, v98
	v_pk_fma_f32 v[82:83], v[184:185], s[2:3], v[82:83] op_sel_hi:[1,1,0]
	v_cndmask_b32_e32 v91, v243, v91, vcc
	v_cmp_ne_u32_e32 vcc, 0, v99
	v_and_b32_e32 v99, 0x800, v98
	s_nop 0
	v_cndmask_b32_e32 v90, v243, v90, vcc
	v_cmp_ne_u32_e32 vcc, 0, v99
	v_and_b32_e32 v99, 0x400, v98
	s_nop 0
	v_cndmask_b32_e32 v89, v243, v89, vcc
	v_cmp_ne_u32_e32 vcc, 0, v99
	v_and_b32_e32 v99, 0x200, v98
	s_nop 0
	v_cndmask_b32_e32 v88, v243, v88, vcc
	v_cmp_ne_u32_e32 vcc, 0, v99
	v_and_b32_e32 v99, 0x100, v98
	s_nop 0
	v_cndmask_b32_e32 v87, v243, v87, vcc
	v_cmp_ne_u32_e32 vcc, 0, v99
	v_and_b32_e32 v99, 8, v98
	s_nop 0
	v_cndmask_b32_e32 v86, v243, v86, vcc
	v_cmp_ne_u32_e32 vcc, 0, v99
	v_and_b32_e32 v99, 4, v98
	s_nop 0
	v_cndmask_b32_e32 v85, v243, v85, vcc
	v_cmp_ne_u32_e32 vcc, 0, v99
	v_and_b32_e32 v99, 2, v98
	v_and_b32_e32 v98, 1, v98
	v_cndmask_b32_e32 v84, v243, v84, vcc
	v_cmp_ne_u32_e32 vcc, 0, v99
	s_nop 1
	v_cndmask_b32_e32 v83, v243, v83, vcc
	v_cmp_eq_u32_e32 vcc, 1, v98
	s_nop 1
	v_cndmask_b32_e32 v82, v243, v82, vcc
	s_setprio 1
	ds_read_b128 v[98:101], v211 offset:49152
	ds_read_b128 v[102:105], v211 offset:57344
	ds_read_b128 v[106:109], v212 offset:49152
	ds_read_b128 v[110:113], v212 offset:57344
	s_waitcnt lgkmcnt(3)
	v_mfma_f32_32x32x16_bf16 v[66:81], v[98:101], v[158:161], v[66:81]
	ds_read_b128 v[98:101], v213 offset:49152
	s_waitcnt lgkmcnt(3)
	v_mfma_f32_32x32x16_bf16 v[82:97], v[102:105], v[158:161], v[82:97]
	ds_read_b128 v[102:105], v213 offset:57344
	s_waitcnt lgkmcnt(3)
	v_mfma_f32_32x32x16_bf16 v[66:81], v[106:109], v[154:157], v[66:81]
	ds_read_b128 v[106:109], v214 offset:49152
	s_waitcnt lgkmcnt(3)
	v_mfma_f32_32x32x16_bf16 v[82:97], v[110:113], v[154:157], v[82:97]
	ds_read_b128 v[110:113], v214 offset:57344
	s_waitcnt lgkmcnt(3)
	v_mfma_f32_32x32x16_bf16 v[66:81], v[98:101], v[150:153], v[66:81]
	ds_read_b128 v[98:101], v211 offset:49280
	s_waitcnt lgkmcnt(3)
	v_mfma_f32_32x32x16_bf16 v[82:97], v[102:105], v[150:153], v[82:97]
	ds_read_b128 v[102:105], v211 offset:57472
	s_waitcnt lgkmcnt(3)
	v_mfma_f32_32x32x16_bf16 v[66:81], v[106:109], v[146:149], v[66:81]
	ds_read_b128 v[106:109], v212 offset:49280
	s_waitcnt lgkmcnt(3)
	v_mfma_f32_32x32x16_bf16 v[82:97], v[110:113], v[146:149], v[82:97]
	ds_read_b128 v[110:113], v212 offset:57472
	s_waitcnt lgkmcnt(3)
	v_mfma_f32_32x32x16_bf16 v[66:81], v[98:101], v[142:145], v[66:81]
	ds_read_b128 v[98:101], v213 offset:49280
	s_waitcnt lgkmcnt(3)
	v_mfma_f32_32x32x16_bf16 v[82:97], v[102:105], v[142:145], v[82:97]
	ds_read_b128 v[102:105], v213 offset:57472
	s_waitcnt lgkmcnt(3)
	v_mfma_f32_32x32x16_bf16 v[66:81], v[106:109], v[138:141], v[66:81]
	ds_read_b128 v[106:109], v214 offset:49280
	s_waitcnt lgkmcnt(3)
	v_mfma_f32_32x32x16_bf16 v[82:97], v[110:113], v[138:141], v[82:97]
	ds_read_b128 v[110:113], v214 offset:57472
	s_waitcnt lgkmcnt(3)
	v_mfma_f32_32x32x16_bf16 v[66:81], v[98:101], v[134:137], v[66:81]
	s_waitcnt lgkmcnt(2)
	v_mfma_f32_32x32x16_bf16 v[82:97], v[102:105], v[134:137], v[82:97]
	s_waitcnt lgkmcnt(1)
	v_mfma_f32_32x32x16_bf16 v[66:81], v[106:109], v[130:133], v[66:81]
	s_waitcnt lgkmcnt(0)
	v_mfma_f32_32x32x16_bf16 v[82:97], v[110:113], v[130:133], v[82:97]
	s_setprio 0
	global_load_dwordx2 v[196:197], v[194:195], off
	v_add_f32_e32 v98, 0, v225
	v_add_f32_e32 v98, v229, v98
	v_add_f32_e32 v98, v226, v98
	v_add_f32_e32 v98, v230, v98
	v_add_f32_e32 v98, v227, v98
	v_add_f32_e32 v98, v231, v98
	v_add_f32_e32 v98, v228, v98
	v_add_f32_e32 v98, v232, v98
	v_add_f32_e32 v98, v173, v98
	v_add_f32_e32 v98, v177, v98
	v_add_f32_e32 v98, v174, v98
	v_add_f32_e32 v98, v222, v98
	v_exp_f32_e32 v106, v170
	v_add_f32_e32 v98, v175, v98
	v_exp_f32_e32 v107, v171
	v_add_f32_e32 v98, v223, v98
	v_exp_f32_e32 v108, v168
	v_add_f32_e32 v98, v176, v98
	v_exp_f32_e32 v109, v169
	v_add_f32_e32 v98, v224, v98
	v_exp_f32_e32 v110, v166
	v_add_f32_e32 v98, v106, v98
	v_exp_f32_e32 v111, v167
	v_add_f32_e32 v98, v107, v98
	v_exp_f32_e32 v112, v164
	v_add_f32_e32 v98, v108, v98
	v_exp_f32_e32 v113, v165
	v_add_f32_e32 v98, v109, v98
	v_exp_f32_e32 v114, v162
	v_add_f32_e32 v98, v110, v98
	v_exp_f32_e32 v115, v163
	v_add_f32_e32 v98, v111, v98
	v_exp_f32_e32 v116, v122
	v_add_f32_e32 v98, v112, v98
	v_exp_f32_e32 v117, v123
	v_add_f32_e32 v98, v113, v98
	v_exp_f32_e32 v120, v120
	v_add_f32_e32 v98, v114, v98
	v_exp_f32_e32 v121, v121
	v_add_f32_e32 v98, v115, v98
	v_exp_f32_e32 v118, v118
	v_add_f32_e32 v98, v116, v98
	v_exp_f32_e32 v119, v119
	v_add_f32_e32 v98, v117, v98
	v_add_f32_e32 v98, v120, v98
	v_add_f32_e32 v98, v121, v98
	v_add_f32_e32 v98, v118, v98
	v_add_f32_e32 v219, v119, v98
	v_mov_b32_e32 v220, v219
	s_nop 1
	v_permlane32_swap_b32_e32 v219, v220
	v_cvt_pk_bf16_f32 v98, v225, v229
	v_cvt_pk_bf16_f32 v99, v226, v230
	v_cvt_pk_bf16_f32 v100, v227, v231
	v_cvt_pk_bf16_f32 v101, v228, v232
	v_cvt_pk_bf16_f32 v102, v173, v177
	v_cvt_pk_bf16_f32 v103, v174, v222
	v_cvt_pk_bf16_f32 v104, v175, v223
	v_cvt_pk_bf16_f32 v105, v176, v224
	v_cvt_pk_bf16_f32 v106, v106, v107
	v_cvt_pk_bf16_f32 v107, v108, v109
	v_cvt_pk_bf16_f32 v108, v110, v111
	v_cvt_pk_bf16_f32 v109, v112, v113
	v_cvt_pk_bf16_f32 v110, v114, v115
	v_cvt_pk_bf16_f32 v111, v116, v117
	v_cvt_pk_bf16_f32 v112, v120, v121
	v_cvt_pk_bf16_f32 v113, v118, v119
	s_nop 0
	v_permlane32_swap_b32_e32 v98, v100
	v_permlane32_swap_b32_e32 v99, v101
	v_permlane32_swap_b32_e32 v102, v104
	v_permlane32_swap_b32_e32 v103, v105
	v_permlane32_swap_b32_e32 v106, v108
	v_permlane32_swap_b32_e32 v107, v109
	v_permlane32_swap_b32_e32 v110, v112
	v_permlane32_swap_b32_e32 v111, v113
	v_mad_i64_i32 v[114:115], s[2:3], v217, s84, v[190:191]
	v_add_u32_e32 v118, 32, v217
	v_mad_i64_i32 v[116:117], s[2:3], v118, s84, v[190:191]
	global_load_dwordx4 v[162:165], v[114:115], off
	global_load_dwordx4 v[166:169], v[116:117], off
	v_mad_i64_i32 v[114:115], s[2:3], v217, s84, v[192:193]
	v_mad_i64_i32 v[116:117], s[2:3], v118, s84, v[192:193]
	global_load_dwordx4 v[170:173], v[114:115], off
	global_load_dwordx4 v[174:177], v[116:117], off
	s_setprio 1
	ds_read_b64_tr_b16 v[114:115], v201 offset:0
	ds_read_b64_tr_b16 v[116:117], v201 offset:0x800
	ds_read_b64_tr_b16 v[118:119], v201 offset:0x1000
	ds_read_b64_tr_b16 v[120:121], v201 offset:0x1800
	ds_read_b64_tr_b16 v[122:123], v201 offset:0x2000
	ds_read_b64_tr_b16 v[124:125], v201 offset:0x2800
	ds_read_b64_tr_b16 v[126:127], v201 offset:0x3000
	ds_read_b64_tr_b16 v[128:129], v201 offset:0x3800
	s_waitcnt lgkmcnt(0)
	s_nop 0
	v_mfma_f32_32x32x16_bf16 v[2:17], v[98:101], v[114:117], v[2:17]
	ds_read_b64_tr_b16 v[114:115], v201 offset:0x200
	ds_read_b64_tr_b16 v[116:117], v201 offset:0xa00
	v_mfma_f32_32x32x16_bf16 v[2:17], v[102:105], v[118:121], v[2:17]
	ds_read_b64_tr_b16 v[118:119], v201 offset:0x1200
	ds_read_b64_tr_b16 v[120:121], v201 offset:0x1a00
	v_mfma_f32_32x32x16_bf16 v[2:17], v[106:109], v[122:125], v[2:17]
	ds_read_b64_tr_b16 v[122:123], v201 offset:0x2200
	ds_read_b64_tr_b16 v[124:125], v201 offset:0x2a00
	v_mfma_f32_32x32x16_bf16 v[2:17], v[110:113], v[126:129], v[2:17]
	ds_read_b64_tr_b16 v[126:127], v201 offset:0x3200
	ds_read_b64_tr_b16 v[128:129], v201 offset:0x3a00
	s_waitcnt lgkmcnt(0)
	v_mfma_f32_32x32x16_bf16 v[50:65], v[98:101], v[114:117], v[50:65]
	ds_read_b64_tr_b16 v[114:115], v201 offset:0x400
	ds_read_b64_tr_b16 v[116:117], v201 offset:0xc00
	v_mfma_f32_32x32x16_bf16 v[50:65], v[102:105], v[118:121], v[50:65]
	ds_read_b64_tr_b16 v[118:119], v201 offset:0x1400
	ds_read_b64_tr_b16 v[120:121], v201 offset:0x1c00
	v_mfma_f32_32x32x16_bf16 v[50:65], v[106:109], v[122:125], v[50:65]
	ds_read_b64_tr_b16 v[122:123], v201 offset:0x2400
	ds_read_b64_tr_b16 v[124:125], v201 offset:0x2c00
	v_mfma_f32_32x32x16_bf16 v[50:65], v[110:113], v[126:129], v[50:65]
	ds_read_b64_tr_b16 v[126:127], v201 offset:0x3400
	ds_read_b64_tr_b16 v[128:129], v201 offset:0x3c00
	s_waitcnt lgkmcnt(0)
	v_mfma_f32_32x32x16_bf16 v[34:49], v[98:101], v[114:117], v[34:49]
	ds_read_b64_tr_b16 v[114:115], v201 offset:0x600
	ds_read_b64_tr_b16 v[116:117], v201 offset:0xe00
	v_mfma_f32_32x32x16_bf16 v[34:49], v[102:105], v[118:121], v[34:49]
	ds_read_b64_tr_b16 v[118:119], v201 offset:0x1600
	ds_read_b64_tr_b16 v[120:121], v201 offset:0x1e00
	v_mfma_f32_32x32x16_bf16 v[34:49], v[106:109], v[122:125], v[34:49]
	ds_read_b64_tr_b16 v[122:123], v201 offset:0x2600
	ds_read_b64_tr_b16 v[124:125], v201 offset:0x2e00
	v_mfma_f32_32x32x16_bf16 v[34:49], v[110:113], v[126:129], v[34:49]
	ds_read_b64_tr_b16 v[126:127], v201 offset:0x3600
	ds_read_b64_tr_b16 v[128:129], v201 offset:0x3e00
	s_waitcnt lgkmcnt(0)
	v_mfma_f32_32x32x16_bf16 v[18:33], v[98:101], v[114:117], v[18:33]
	v_mfma_f32_32x32x16_bf16 v[18:33], v[102:105], v[118:121], v[18:33]
	v_mfma_f32_32x32x16_bf16 v[18:33], v[106:109], v[122:125], v[18:33]
	v_mfma_f32_32x32x16_bf16 v[18:33], v[110:113], v[126:129], v[18:33]
	s_setprio 0
	v_max_f32_e32 v98, v67, v67
	v_max_f32_e32 v99, v66, v66
	v_max_f32_e32 v98, v99, v98
	v_max3_f32 v98, v98, v68, v69
	v_max3_f32 v98, v98, v70, v71
	v_max3_f32 v98, v98, v72, v73
	v_max3_f32 v98, v98, v74, v75
	v_max3_f32 v98, v98, v76, v77
	v_max3_f32 v98, v98, v78, v79
	v_max3_f32 v98, v98, v80, v81
	v_max3_f32 v98, v98, v82, v83
	v_max3_f32 v98, v98, v84, v85
	v_max3_f32 v98, v98, v86, v87
	v_max3_f32 v98, v98, v88, v89
	v_max3_f32 v98, v98, v90, v91
	v_max3_f32 v98, v98, v92, v93
	v_max3_f32 v98, v98, v94, v95
	v_max3_f32 v98, v98, v96, v97
	v_mov_b32_e32 v99, v98
	s_nop 1
	v_permlane32_swap_b32_e32 v98, v99
	v_max_f32_e32 v99, v99, v99
	v_max_f32_e32 v98, v98, v98
	v_max_f32_e32 v98, v98, v99
	v_sub_f32_e32 v99, v98, v215
	v_mul_f32_e32 v99, 0x3db504f3, v99
	v_cmp_ge_f32_e32 vcc, s74, v99
	v_max_f32_e32 v99, v215, v215
	v_max_f32_e32 v222, v99, v98
	v_sub_f32_e32 v98, v215, v222
	v_mul_f32_e32 v98, 0x3e0293ee, v98
	v_exp_f32_e32 v98, v98
	s_cmp_eq_u64 vcc, exec
	s_waitcnt lgkmcnt(0)
	s_barrier
	s_cselect_b64 s[2:3], -1, 0
	s_waitcnt vmcnt(0)
	v_cndmask_b32_e64 v221, v98, 1.0, s[2:3]
	v_cmp_gt_f32_e32 vcc, 1.0, v221
	s_waitcnt vmcnt(3)
	ds_write_b128 v210, v[162:165]
	s_waitcnt vmcnt(2)
	ds_write_b128 v210, v[166:169] offset:8192
	s_waitcnt vmcnt(1)
	ds_write_b128 v204, v[170:173] offset:32768
	s_waitcnt vmcnt(0)
	ds_write_b128 v204, v[174:177] offset:40960
	s_cbranch_vccz .LBB0_1147
	s_and_saveexec_b64 s[4:5], s[0:1]
	ds_write_b32 v206, v221 offset:128
	s_or_b64 exec, exec, s[4:5]
	s_waitcnt lgkmcnt(0)
	ds_read_b128 v[98:101], v205 offset:224
	ds_read_b128 v[102:105], v205 offset:192
	ds_read_b128 v[106:109], v205 offset:160
	ds_read_b128 v[110:113], v205 offset:128
	v_readlane_b32 s56, v254, 33
	s_waitcnt lgkmcnt(3)
	v_pk_mul_f32 v[16:17], v[16:17], v[100:101]
	s_waitcnt lgkmcnt(2)
	v_pk_mul_f32 v[12:13], v[12:13], v[104:105]
	s_waitcnt lgkmcnt(1)
	v_pk_mul_f32 v[8:9], v[8:9], v[108:109]
	s_waitcnt lgkmcnt(0)
	v_pk_mul_f32 v[4:5], v[4:5], v[112:113]
	v_pk_mul_f32 v[14:15], v[14:15], v[98:99]
	v_pk_mul_f32 v[10:11], v[10:11], v[102:103]
	v_pk_mul_f32 v[6:7], v[6:7], v[106:107]
	v_pk_mul_f32 v[2:3], v[2:3], v[110:111]
	v_pk_mul_f32 v[64:65], v[64:65], v[100:101]
	v_pk_mul_f32 v[60:61], v[60:61], v[104:105]
	v_pk_mul_f32 v[56:57], v[56:57], v[108:109]
	v_pk_mul_f32 v[52:53], v[52:53], v[112:113]
	v_pk_mul_f32 v[62:63], v[62:63], v[98:99]
	v_pk_mul_f32 v[58:59], v[58:59], v[102:103]
	v_pk_mul_f32 v[54:55], v[54:55], v[106:107]
	v_pk_mul_f32 v[50:51], v[50:51], v[110:111]
	v_pk_mul_f32 v[48:49], v[48:49], v[100:101]
	v_pk_mul_f32 v[44:45], v[44:45], v[104:105]
	v_pk_mul_f32 v[40:41], v[40:41], v[108:109]
	v_pk_mul_f32 v[36:37], v[36:37], v[112:113]
	v_pk_mul_f32 v[46:47], v[46:47], v[98:99]
	v_pk_mul_f32 v[42:43], v[42:43], v[102:103]
	v_pk_mul_f32 v[38:39], v[38:39], v[106:107]
	v_pk_mul_f32 v[34:35], v[34:35], v[110:111]
	v_pk_mul_f32 v[32:33], v[32:33], v[100:101]
	v_pk_mul_f32 v[28:29], v[28:29], v[104:105]
	v_pk_mul_f32 v[24:25], v[24:25], v[108:109]
	v_pk_mul_f32 v[20:21], v[20:21], v[112:113]
	v_pk_mul_f32 v[30:31], v[30:31], v[98:99]
	v_pk_mul_f32 v[26:27], v[26:27], v[102:103]
	v_pk_mul_f32 v[22:23], v[22:23], v[106:107]
	v_pk_mul_f32 v[18:19], v[18:19], v[110:111]
	v_readlane_b32 s57, v254, 34
.LBB0_1147:
	s_waitcnt lgkmcnt(0)
	s_barrier
	v_cvt_f32_i32_e32 v99, v216
	v_lshrrev_b32_e32 v115, v208, v196
	v_and_b32_e32 v98, 1, v115
	v_cmp_eq_u32_e32 vcc, 1, v98
	v_mul_f32_e64 v114, -v178, v99
	v_fma_f32 v100, 0, v178, v114
	v_cndmask_b32_e32 v98, v243, v100, vcc
	v_and_b32_e32 v100, 2, v115
	v_fma_f32 v99, -v178, v99, v178
	v_cmp_ne_u32_e32 vcc, 0, v100
	v_and_b32_e32 v102, 8, v115
	v_pk_fma_f32 v[100:101], v[188:189], s[60:61], v[114:115] op_sel_hi:[1,1,0]
	v_cndmask_b32_e32 v99, v243, v99, vcc
	v_and_b32_e32 v103, 4, v115
	v_cmp_ne_u32_e32 vcc, 0, v102
	v_and_b32_e32 v104, 0x200, v115
	v_and_b32_e32 v105, 0x100, v115
	v_cndmask_b32_e32 v101, v243, v101, vcc
	v_cmp_ne_u32_e32 vcc, 0, v103
	v_pk_fma_f32 v[102:103], v[188:189], s[74:75], v[114:115] op_sel_hi:[1,1,0]
	v_and_b32_e32 v106, 0x800, v115
	v_cndmask_b32_e32 v100, v243, v100, vcc
	v_cmp_ne_u32_e32 vcc, 0, v104
	v_and_b32_e32 v107, 0x400, v115
	v_and_b32_e32 v108, 0x20000, v115
	v_cndmask_b32_e32 v103, v243, v103, vcc
	v_cmp_ne_u32_e32 vcc, 0, v105
	v_pk_fma_f32 v[104:105], v[188:189], s[62:63], v[114:115] op_sel_hi:[1,1,0]
	v_and_b32_e32 v109, 0x10000, v115
	v_cndmask_b32_e32 v102, v243, v102, vcc
	v_cmp_ne_u32_e32 vcc, 0, v106
	s_mov_b32 s4, 0x41900000
	s_mov_b32 s5, 0x41980000
	v_cndmask_b32_e32 v105, v243, v105, vcc
	v_cmp_ne_u32_e32 vcc, 0, v107
	v_pk_fma_f32 v[106:107], v[188:189], s[58:59], v[114:115] op_sel_hi:[1,1,0]
	v_and_b32_e32 v110, 0x80000, v115
	v_cndmask_b32_e32 v104, v243, v104, vcc
	v_cmp_ne_u32_e32 vcc, 0, v108
	v_and_b32_e32 v111, 0x40000, v115
	v_and_b32_e32 v112, 0x2000000, v115
	v_cndmask_b32_e32 v107, v243, v107, vcc
	v_cmp_ne_u32_e32 vcc, 0, v109
	v_pk_fma_f32 v[108:109], v[188:189], s[4:5], v[114:115] op_sel_hi:[1,1,0]
	s_mov_b32 s4, 0x41c00000
	v_cndmask_b32_e32 v106, v243, v106, vcc
	v_cmp_ne_u32_e32 vcc, 0, v110
	s_mov_b32 s5, 0x41c80000
	v_and_b32_e32 v113, 0x1000000, v115
	v_cndmask_b32_e32 v109, v243, v109, vcc
	v_cmp_ne_u32_e32 vcc, 0, v111
	v_pk_fma_f32 v[110:111], v[188:189], s[4:5], v[114:115] op_sel_hi:[1,1,0]
	s_mov_b32 s4, 0x41d00000
	v_cndmask_b32_e32 v108, v243, v108, vcc
	v_cmp_ne_u32_e32 vcc, 0, v112
	s_mov_b32 s5, 0x41d80000
	v_and_b32_e32 v116, 0x8000000, v115
	v_cndmask_b32_e32 v111, v243, v111, vcc
	v_cmp_ne_u32_e32 vcc, 0, v113
	v_lshrrev_b32_e32 v223, v208, v197
	v_pk_fma_f32 v[112:113], v[188:189], s[4:5], v[114:115] op_sel_hi:[1,1,0]
	v_cndmask_b32_e32 v110, v243, v110, vcc
	v_and_b32_e32 v115, 0x4000000, v115
	v_cmp_ne_u32_e32 vcc, 0, v116
	v_mov_b32_e32 v179, v178
	v_pk_fma_f32 v[116:117], v[178:179], s[86:87], v[114:115] op_sel_hi:[1,1,0]
	v_cndmask_b32_e32 v113, v243, v113, vcc
	v_cmp_ne_u32_e32 vcc, 0, v115
	v_pk_fma_f32 v[118:119], v[178:179], s[88:89], v[114:115] op_sel_hi:[1,1,0]
	v_pk_fma_f32 v[120:121], v[178:179], s[90:91], v[114:115] op_sel_hi:[1,1,0]
	v_pk_fma_f32 v[122:123], v[178:179], s[92:93], v[114:115] op_sel_hi:[1,1,0]
	v_pk_fma_f32 v[124:125], v[178:179], s[94:95], v[114:115] op_sel_hi:[1,1,0]
	v_pk_fma_f32 v[126:127], v[178:179], s[96:97], v[114:115] op_sel_hi:[1,1,0]
	v_pk_fma_f32 v[128:129], v[178:179], s[68:69], v[114:115] op_sel_hi:[1,1,0]
	v_and_b32_e32 v179, 0x8000000, v223
	v_cndmask_b32_e32 v112, v243, v112, vcc
	v_cmp_ne_u32_e32 vcc, 0, v179
	v_and_b32_e32 v179, 0x4000000, v223
	s_mov_b32 s4, 0x42000000
	v_cndmask_b32_e32 v129, v243, v129, vcc
	v_cmp_ne_u32_e32 vcc, 0, v179
	v_and_b32_e32 v179, 0x2000000, v223
	s_mov_b32 s5, 0x42040000
	v_cndmask_b32_e32 v128, v243, v128, vcc
	v_cmp_ne_u32_e32 vcc, 0, v179
	v_and_b32_e32 v179, 0x1000000, v223
	v_pk_fma_f32 v[114:115], v[184:185], s[4:5], v[114:115] op_sel_hi:[1,1,0]
	v_cndmask_b32_e32 v127, v243, v127, vcc
	v_cmp_ne_u32_e32 vcc, 0, v179
	v_and_b32_e32 v179, 0x80000, v223
	s_nop 0
	v_cndmask_b32_e32 v126, v243, v126, vcc
	v_cmp_ne_u32_e32 vcc, 0, v179
	v_and_b32_e32 v179, 0x40000, v223
	s_nop 0
	v_cndmask_b32_e32 v125, v243, v125, vcc
	v_cmp_ne_u32_e32 vcc, 0, v179
	v_and_b32_e32 v179, 0x20000, v223
	s_nop 0
	v_cndmask_b32_e32 v124, v243, v124, vcc
	v_cmp_ne_u32_e32 vcc, 0, v179
	v_and_b32_e32 v179, 0x10000, v223
	s_nop 0
	v_cndmask_b32_e32 v123, v243, v123, vcc
	v_cmp_ne_u32_e32 vcc, 0, v179
	v_and_b32_e32 v179, 0x800, v223
	s_nop 0
	v_cndmask_b32_e32 v122, v243, v122, vcc
	v_cmp_ne_u32_e32 vcc, 0, v179
	v_and_b32_e32 v179, 0x400, v223
	s_nop 0
	v_cndmask_b32_e32 v121, v243, v121, vcc
	v_cmp_ne_u32_e32 vcc, 0, v179
	v_and_b32_e32 v179, 0x200, v223
	s_nop 0
	v_cndmask_b32_e32 v120, v243, v120, vcc
	v_cmp_ne_u32_e32 vcc, 0, v179
	v_and_b32_e32 v179, 0x100, v223
	s_nop 0
	v_cndmask_b32_e32 v119, v243, v119, vcc
	v_cmp_ne_u32_e32 vcc, 0, v179
	v_and_b32_e32 v179, 8, v223
	s_nop 0
	v_cndmask_b32_e32 v118, v243, v118, vcc
	v_cmp_ne_u32_e32 vcc, 0, v179
	v_and_b32_e32 v179, 4, v223
	s_nop 0
	v_cndmask_b32_e32 v117, v243, v117, vcc
	v_cmp_ne_u32_e32 vcc, 0, v179
	v_and_b32_e32 v179, 2, v223
	s_nop 0
	v_cndmask_b32_e32 v116, v243, v116, vcc
	v_cmp_ne_u32_e32 vcc, 0, v179
	v_and_b32_e32 v179, 1, v223
	s_nop 0
	v_cndmask_b32_e32 v115, v243, v115, vcc
	v_cmp_eq_u32_e32 vcc, 1, v179
	s_nop 1
	v_cndmask_b32_e32 v114, v243, v114, vcc
	s_setprio 1
	ds_read_b128 v[224:227], v211 offset:32768
	ds_read_b128 v[228:231], v211 offset:40960
	s_waitcnt lgkmcnt(1)
	v_mfma_f32_32x32x16_bf16 v[98:113], v[224:227], v[158:161], v[98:113]
	ds_read_b128 v[224:227], v212 offset:32768
	s_waitcnt lgkmcnt(1)
	v_mfma_f32_32x32x16_bf16 v[114:129], v[228:231], v[158:161], v[114:129]
	ds_read_b128 v[228:231], v212 offset:40960
	s_waitcnt lgkmcnt(1)
	v_mfma_f32_32x32x16_bf16 v[98:113], v[224:227], v[154:157], v[98:113]
	ds_read_b128 v[224:227], v213 offset:32768
	s_waitcnt lgkmcnt(1)
	v_mfma_f32_32x32x16_bf16 v[114:129], v[228:231], v[154:157], v[114:129]
	ds_read_b128 v[228:231], v213 offset:40960
	s_waitcnt lgkmcnt(1)
	v_mfma_f32_32x32x16_bf16 v[98:113], v[224:227], v[150:153], v[98:113]
	ds_read_b128 v[224:227], v214 offset:32768
	s_waitcnt lgkmcnt(1)
	v_mfma_f32_32x32x16_bf16 v[114:129], v[228:231], v[150:153], v[114:129]
	ds_read_b128 v[228:231], v214 offset:40960
	s_waitcnt lgkmcnt(1)
	v_mfma_f32_32x32x16_bf16 v[98:113], v[224:227], v[146:149], v[98:113]
	ds_read_b128 v[224:227], v211 offset:32896
	s_waitcnt lgkmcnt(1)
	v_mfma_f32_32x32x16_bf16 v[114:129], v[228:231], v[146:149], v[114:129]
	ds_read_b128 v[228:231], v211 offset:41088
	s_waitcnt lgkmcnt(1)
	v_mfma_f32_32x32x16_bf16 v[98:113], v[224:227], v[142:145], v[98:113]
	ds_read_b128 v[224:227], v212 offset:32896
	s_waitcnt lgkmcnt(1)
	v_mfma_f32_32x32x16_bf16 v[114:129], v[228:231], v[142:145], v[114:129]
	ds_read_b128 v[228:231], v212 offset:41088
	s_waitcnt lgkmcnt(1)
	v_mfma_f32_32x32x16_bf16 v[98:113], v[224:227], v[138:141], v[98:113]
	ds_read_b128 v[224:227], v213 offset:32896
	s_waitcnt lgkmcnt(1)
	v_mfma_f32_32x32x16_bf16 v[114:129], v[228:231], v[138:141], v[114:129]
	ds_read_b128 v[228:231], v213 offset:41088
	s_waitcnt lgkmcnt(1)
	v_mfma_f32_32x32x16_bf16 v[98:113], v[224:227], v[134:137], v[98:113]
	ds_read_b128 v[224:227], v214 offset:32896
	s_waitcnt lgkmcnt(1)
	v_mfma_f32_32x32x16_bf16 v[114:129], v[228:231], v[134:137], v[114:129]
	ds_read_b128 v[228:231], v214 offset:41088
	s_waitcnt lgkmcnt(1)
	v_mfma_f32_32x32x16_bf16 v[98:113], v[224:227], v[130:133], v[98:113]
	s_waitcnt lgkmcnt(0)
	v_mfma_f32_32x32x16_bf16 v[114:129], v[228:231], v[130:133], v[114:129]
	s_setprio 0
	s_add_i32 s55, s53, 1
	s_cmp_lt_u32 s55, s54
	s_cselect_b64 s[4:5], -1, 0
	s_cmp_ge_u32 s55, s54
	s_cbranch_scc1 .LBB0_1149
	global_load_dwordx2 v[196:197], v[194:195], off offset:8

.LBB0_1260:
	v_add_u32_e32 v146, 64, v199
	v_cvt_f32_i32_e32 v66, v146
	s_sub_i32 s2, s85, 63
	s_lshr_b32 s2, s2, 8
	v_lshrrev_b32_sdwa v67, s2, v192 dst_sel:DWORD dst_unused:UNUSED_PAD src0_sel:DWORD src1_sel:WORD_0
	v_and_b32_e32 v67, 1, v67
	v_mul_f32_e64 v66, -v162, v66
	v_cmp_eq_u32_e32 vcc, 1, v67
	s_mov_b32 s2, 0x41900000
	s_mov_b32 s3, 0x41980000
	v_cndmask_b32_e32 v82, v243, v66, vcc
	v_pk_fma_f32 v[76:77], v[170:171], s[2:3], v[82:83] op_sel_hi:[1,1,0]
	s_mov_b32 s2, 0x41c00000
	s_mov_b32 s3, 0x41c80000
	v_pk_fma_f32 v[78:79], v[170:171], s[2:3], v[82:83] op_sel_hi:[1,1,0]
	s_mov_b32 s2, 0x41d00000
	s_mov_b32 s3, 0x41d80000
	v_pk_fma_f32 v[80:81], v[170:171], s[2:3], v[82:83] op_sel_hi:[1,1,0]
	s_mov_b32 s2, 0x42000000
	s_mov_b32 s3, 0x42040000
	v_fma_f32 v66, 0, v162, v82
	v_add_f32_e32 v67, v162, v82
	v_pk_fma_f32 v[68:69], v[170:171], s[60:61], v[82:83] op_sel_hi:[1,1,0]
	v_pk_fma_f32 v[70:71], v[170:171], s[74:75], v[82:83] op_sel_hi:[1,1,0]
	v_pk_fma_f32 v[72:73], v[170:171], s[62:63], v[82:83] op_sel_hi:[1,1,0]
	v_pk_fma_f32 v[74:75], v[170:171], s[58:59], v[82:83] op_sel_hi:[1,1,0]
	v_pk_fma_f32 v[96:97], v[170:171], s[68:69], v[82:83] op_sel_hi:[1,1,0]
	v_pk_fma_f32 v[94:95], v[170:171], s[96:97], v[82:83] op_sel_hi:[1,1,0]
	v_pk_fma_f32 v[92:93], v[170:171], s[94:95], v[82:83] op_sel_hi:[1,1,0]
	v_pk_fma_f32 v[90:91], v[170:171], s[92:93], v[82:83] op_sel_hi:[1,1,0]
	v_pk_fma_f32 v[88:89], v[170:171], s[90:91], v[82:83] op_sel_hi:[1,1,0]
	v_pk_fma_f32 v[86:87], v[170:171], s[88:89], v[82:83] op_sel_hi:[1,1,0]
	v_pk_fma_f32 v[84:85], v[170:171], s[86:87], v[82:83] op_sel_hi:[1,1,0]
	v_pk_fma_f32 v[82:83], v[168:169], s[2:3], v[82:83] op_sel_hi:[1,1,0]
	s_setprio 1
	ds_read_b128 v[130:133], v195 offset:49152
	ds_read_b128 v[134:137], v195 offset:57344
	ds_read_b128 v[138:141], v196 offset:49152
	ds_read_b128 v[142:145], v196 offset:57344
	s_waitcnt lgkmcnt(3)
	v_mfma_f32_32x32x16_bf16 v[66:81], v[130:133], v[126:129], v[66:81]
	ds_read_b128 v[130:133], v197 offset:49152
	s_waitcnt lgkmcnt(3)
	v_mfma_f32_32x32x16_bf16 v[82:97], v[134:137], v[126:129], v[82:97]
	ds_read_b128 v[134:137], v197 offset:57344
	s_waitcnt lgkmcnt(3)
	v_mfma_f32_32x32x16_bf16 v[66:81], v[138:141], v[122:125], v[66:81]
	ds_read_b128 v[138:141], v198 offset:49152
	s_waitcnt lgkmcnt(3)
	v_mfma_f32_32x32x16_bf16 v[82:97], v[142:145], v[122:125], v[82:97]
	ds_read_b128 v[142:145], v198 offset:57344
	s_waitcnt lgkmcnt(3)
	v_mfma_f32_32x32x16_bf16 v[66:81], v[130:133], v[118:121], v[66:81]
	ds_read_b128 v[130:133], v195 offset:49280
	s_waitcnt lgkmcnt(3)
	v_mfma_f32_32x32x16_bf16 v[82:97], v[134:137], v[118:121], v[82:97]
	ds_read_b128 v[134:137], v195 offset:57472
	s_waitcnt lgkmcnt(3)
	v_mfma_f32_32x32x16_bf16 v[66:81], v[138:141], v[114:117], v[66:81]
	ds_read_b128 v[138:141], v196 offset:49280
	s_waitcnt lgkmcnt(3)
	v_mfma_f32_32x32x16_bf16 v[82:97], v[142:145], v[114:117], v[82:97]
	ds_read_b128 v[142:145], v196 offset:57472
	s_waitcnt lgkmcnt(3)
	v_mfma_f32_32x32x16_bf16 v[66:81], v[130:133], v[110:113], v[66:81]
	ds_read_b128 v[130:133], v197 offset:49280
	s_waitcnt lgkmcnt(3)
	v_mfma_f32_32x32x16_bf16 v[82:97], v[134:137], v[110:113], v[82:97]
	ds_read_b128 v[134:137], v197 offset:57472
	s_waitcnt lgkmcnt(3)
	v_mfma_f32_32x32x16_bf16 v[66:81], v[138:141], v[106:109], v[66:81]
	ds_read_b128 v[138:141], v198 offset:49280
	s_waitcnt lgkmcnt(3)
	v_mfma_f32_32x32x16_bf16 v[82:97], v[142:145], v[106:109], v[82:97]
	ds_read_b128 v[142:145], v198 offset:57472
	s_waitcnt lgkmcnt(3)
	v_mfma_f32_32x32x16_bf16 v[66:81], v[130:133], v[102:105], v[66:81]
	s_waitcnt lgkmcnt(2)
	v_mfma_f32_32x32x16_bf16 v[82:97], v[134:137], v[102:105], v[82:97]
	s_waitcnt lgkmcnt(1)
	v_mfma_f32_32x32x16_bf16 v[66:81], v[138:141], v[98:101], v[66:81]
	s_waitcnt lgkmcnt(0)
	v_mfma_f32_32x32x16_bf16 v[82:97], v[142:145], v[98:101], v[82:97]
	s_setprio 0
	v_add_f32_e32 v147, 0, v216
	v_add_f32_e32 v147, v220, v147
	v_add_f32_e32 v147, v217, v147
	v_add_f32_e32 v147, v221, v147
	v_add_f32_e32 v147, v218, v147
	v_add_f32_e32 v147, v222, v147
	v_add_f32_e32 v147, v219, v147
	v_add_f32_e32 v147, v223, v147
	v_add_f32_e32 v147, v208, v147
	v_add_f32_e32 v147, v212, v147
	v_add_f32_e32 v147, v209, v147
	v_add_f32_e32 v147, v213, v147
	v_exp_f32_e32 v130, v178
	v_add_f32_e32 v147, v210, v147
	v_exp_f32_e32 v131, v179
	v_add_f32_e32 v147, v214, v147
	v_exp_f32_e32 v132, v176
	v_add_f32_e32 v147, v211, v147
	v_exp_f32_e32 v133, v177
	v_add_f32_e32 v147, v215, v147
	s_waitcnt vmcnt(2)
	v_exp_f32_e32 v134, v160
	v_add_f32_e32 v147, v130, v147
	v_exp_f32_e32 v135, v161
	v_add_f32_e32 v147, v131, v147
	v_exp_f32_e32 v136, v158
	v_add_f32_e32 v147, v132, v147
	v_exp_f32_e32 v137, v159
	v_add_f32_e32 v147, v133, v147
	s_waitcnt vmcnt(1)
	v_exp_f32_e32 v138, v156
	v_add_f32_e32 v147, v134, v147
	v_exp_f32_e32 v139, v157
	v_add_f32_e32 v147, v135, v147
	v_exp_f32_e32 v140, v154
	v_add_f32_e32 v147, v136, v147
	v_exp_f32_e32 v141, v155
	v_add_f32_e32 v147, v137, v147
	s_waitcnt vmcnt(0)
	v_exp_f32_e32 v142, v152
	v_add_f32_e32 v147, v138, v147
	v_exp_f32_e32 v143, v153
	v_add_f32_e32 v147, v139, v147
	v_exp_f32_e32 v144, v150
	v_add_f32_e32 v147, v140, v147
	v_exp_f32_e32 v145, v151
	v_add_f32_e32 v147, v141, v147
	v_add_f32_e32 v147, v142, v147
	v_add_f32_e32 v147, v143, v147
	v_add_f32_e32 v147, v144, v147
	v_add_f32_e32 v204, v145, v147
	v_mov_b32_e32 v205, v204
	s_nop 1
	v_permlane32_swap_b32_e32 v204, v205
	v_cvt_pk_bf16_f32 v148, v216, v220
	v_cvt_pk_bf16_f32 v149, v217, v221
	v_cvt_pk_bf16_f32 v150, v218, v222
	v_cvt_pk_bf16_f32 v151, v219, v223
	v_cvt_pk_bf16_f32 v152, v208, v212
	v_cvt_pk_bf16_f32 v153, v209, v213
	v_cvt_pk_bf16_f32 v154, v210, v214
	v_cvt_pk_bf16_f32 v155, v211, v215
	v_cvt_pk_bf16_f32 v156, v130, v131
	v_cvt_pk_bf16_f32 v157, v132, v133
	v_cvt_pk_bf16_f32 v158, v134, v135
	v_cvt_pk_bf16_f32 v159, v136, v137
	v_cvt_pk_bf16_f32 v206, v138, v139
	v_cvt_pk_bf16_f32 v207, v140, v141
	v_cvt_pk_bf16_f32 v208, v142, v143
	v_cvt_pk_bf16_f32 v209, v144, v145
	s_nop 0
	v_permlane32_swap_b32_e32 v148, v150
	v_permlane32_swap_b32_e32 v149, v151
	v_permlane32_swap_b32_e32 v152, v154
	v_permlane32_swap_b32_e32 v153, v155
	v_permlane32_swap_b32_e32 v156, v158
	v_permlane32_swap_b32_e32 v157, v159
	v_permlane32_swap_b32_e32 v206, v208
	v_permlane32_swap_b32_e32 v207, v209
	v_add_u32_e32 v177, s85, v167
	v_add_u32_e32 v138, 1, v177
	v_add_u32_e32 v140, 33, v177
	v_mad_i64_i32 v[130:131], s[2:3], v138, s71, v[172:173]
	v_mad_i64_i32 v[134:135], s[2:3], v140, s71, v[172:173]
	v_mad_i64_i32 v[138:139], s[2:3], v138, s71, v[174:175]
	v_mad_i64_i32 v[142:143], s[2:3], v140, s71, v[174:175]
	global_load_dwordx4 v[130:133], v[130:131], off
	s_nop 0
	global_load_dwordx4 v[134:137], v[134:135], off
	s_nop 0
	global_load_dwordx4 v[138:141], v[138:139], off
	s_nop 0
	global_load_dwordx4 v[142:145], v[142:143], off
	s_setprio 1
	ds_read_b64_tr_b16 v[210:211], v188 offset:0
	ds_read_b64_tr_b16 v[212:213], v188 offset:0x800
	ds_read_b64_tr_b16 v[214:215], v188 offset:0x1000
	ds_read_b64_tr_b16 v[216:217], v188 offset:0x1800
	ds_read_b64_tr_b16 v[218:219], v188 offset:0x2000
	ds_read_b64_tr_b16 v[220:221], v188 offset:0x2800
	ds_read_b64_tr_b16 v[222:223], v188 offset:0x3000
	ds_read_b64_tr_b16 v[224:225], v188 offset:0x3800
	s_waitcnt lgkmcnt(0)
	s_nop 0
	v_mfma_f32_32x32x16_bf16 v[34:49], v[148:151], v[210:213], v[34:49]
	ds_read_b64_tr_b16 v[210:211], v188 offset:0x200
	ds_read_b64_tr_b16 v[212:213], v188 offset:0xa00
	v_mfma_f32_32x32x16_bf16 v[34:49], v[152:155], v[214:217], v[34:49]
	ds_read_b64_tr_b16 v[214:215], v188 offset:0x1200
	ds_read_b64_tr_b16 v[216:217], v188 offset:0x1a00
	v_mfma_f32_32x32x16_bf16 v[34:49], v[156:159], v[218:221], v[34:49]
	ds_read_b64_tr_b16 v[218:219], v188 offset:0x2200
	ds_read_b64_tr_b16 v[220:221], v188 offset:0x2a00
	v_mfma_f32_32x32x16_bf16 v[34:49], v[206:209], v[222:225], v[34:49]
	ds_read_b64_tr_b16 v[222:223], v188 offset:0x3200
	ds_read_b64_tr_b16 v[224:225], v188 offset:0x3a00
	s_waitcnt lgkmcnt(0)
	v_mfma_f32_32x32x16_bf16 v[50:65], v[148:151], v[210:213], v[50:65]
	ds_read_b64_tr_b16 v[210:211], v188 offset:0x400
	ds_read_b64_tr_b16 v[212:213], v188 offset:0xc00
	v_mfma_f32_32x32x16_bf16 v[50:65], v[152:155], v[214:217], v[50:65]
	ds_read_b64_tr_b16 v[214:215], v188 offset:0x1400
	ds_read_b64_tr_b16 v[216:217], v188 offset:0x1c00
	v_mfma_f32_32x32x16_bf16 v[50:65], v[156:159], v[218:221], v[50:65]
	ds_read_b64_tr_b16 v[218:219], v188 offset:0x2400
	ds_read_b64_tr_b16 v[220:221], v188 offset:0x2c00
	v_mfma_f32_32x32x16_bf16 v[50:65], v[206:209], v[222:225], v[50:65]
	ds_read_b64_tr_b16 v[222:223], v188 offset:0x3400
	ds_read_b64_tr_b16 v[224:225], v188 offset:0x3c00
	s_waitcnt lgkmcnt(0)
	v_mfma_f32_32x32x16_bf16 v[18:33], v[148:151], v[210:213], v[18:33]
	ds_read_b64_tr_b16 v[210:211], v188 offset:0x600
	ds_read_b64_tr_b16 v[212:213], v188 offset:0xe00
	v_mfma_f32_32x32x16_bf16 v[18:33], v[152:155], v[214:217], v[18:33]
	ds_read_b64_tr_b16 v[214:215], v188 offset:0x1600
	ds_read_b64_tr_b16 v[216:217], v188 offset:0x1e00
	v_mfma_f32_32x32x16_bf16 v[18:33], v[156:159], v[218:221], v[18:33]
	ds_read_b64_tr_b16 v[218:219], v188 offset:0x2600
	ds_read_b64_tr_b16 v[220:221], v188 offset:0x2e00
	v_mfma_f32_32x32x16_bf16 v[18:33], v[206:209], v[222:225], v[18:33]
	ds_read_b64_tr_b16 v[222:223], v188 offset:0x3600
	ds_read_b64_tr_b16 v[224:225], v188 offset:0x3e00
	s_waitcnt lgkmcnt(0)
	v_mfma_f32_32x32x16_bf16 v[2:17], v[148:151], v[210:213], v[2:17]
	v_mfma_f32_32x32x16_bf16 v[2:17], v[152:155], v[214:217], v[2:17]
	v_mfma_f32_32x32x16_bf16 v[2:17], v[156:159], v[218:221], v[2:17]
	v_mfma_f32_32x32x16_bf16 v[2:17], v[206:209], v[222:225], v[2:17]
	s_setprio 0
	s_cmp_le_i32 s85, s78
	s_cbranch_scc1 .LBB0_1262
	v_cmp_gt_i32_e64 s[60:61], 26, v146
	v_cmp_gt_i32_e64 s[62:63], 27, v146
	v_cmp_gt_i32_e64 s[58:59], 25, v146
	s_and_b64 s[60:61], s[62:63], s[60:61]
	v_cmp_gt_i32_e64 s[56:57], 24, v146
	s_and_b64 s[58:59], s[60:61], s[58:59]
	v_cmp_gt_i32_e64 s[54:55], 19, v146
	s_and_b64 s[56:57], s[58:59], s[56:57]
	v_cmp_gt_i32_e64 s[52:53], 18, v146
	s_and_b64 s[54:55], s[56:57], s[54:55]
	v_cmp_gt_i32_e64 s[50:51], 17, v146
	s_and_b64 s[52:53], s[54:55], s[52:53]
	v_cmp_gt_i32_e64 s[48:49], 16, v146
	s_and_b64 s[50:51], s[52:53], s[50:51]
	v_cmp_gt_i32_e64 s[46:47], 11, v146
	s_and_b64 s[48:49], s[50:51], s[48:49]
	v_cmp_gt_i32_e64 s[44:45], 10, v146
	s_and_b64 s[46:47], s[48:49], s[46:47]
	v_cmp_gt_i32_e64 s[42:43], 9, v146
	s_and_b64 s[44:45], s[46:47], s[44:45]
	v_cmp_gt_i32_e64 s[40:41], 8, v146
	s_and_b64 s[42:43], s[44:45], s[42:43]
	v_cmp_gt_i32_e64 s[38:39], 3, v146
	s_and_b64 s[40:41], s[42:43], s[40:41]
	v_cmp_gt_i32_e64 s[36:37], 2, v146
	s_and_b64 s[38:39], s[40:41], s[38:39]
	v_cmp_gt_i32_e64 s[34:35], 1, v146
	s_and_b64 s[36:37], s[38:39], s[36:37]
	v_cmp_gt_i32_e64 s[30:31], 0, v146
	s_and_b64 s[34:35], s[36:37], s[34:35]
	s_and_b64 s[30:31], s[34:35], s[30:31]
	v_cmp_gt_i32_e64 s[28:29], 58, v146
	v_cndmask_b32_e64 v66, v66, v243, s[30:31]
	v_cmp_gt_i32_e64 s[30:31], 59, v146
	v_cmp_gt_i32_e64 s[26:27], 57, v146
	s_and_b64 s[28:29], s[30:31], s[28:29]
	v_cmp_gt_i32_e64 s[24:25], 56, v146
	s_and_b64 s[26:27], s[28:29], s[26:27]
	v_cmp_gt_i32_e64 s[22:23], 51, v146
	s_and_b64 s[24:25], s[26:27], s[24:25]
	v_cmp_gt_i32_e64 s[20:21], 50, v146
	s_and_b64 s[22:23], s[24:25], s[22:23]
	v_cmp_gt_i32_e64 s[18:19], 49, v146
	s_and_b64 s[20:21], s[22:23], s[20:21]
	v_cmp_gt_i32_e64 s[16:17], 48, v146
	s_and_b64 s[18:19], s[20:21], s[18:19]
	v_cmp_gt_i32_e64 s[14:15], 43, v146
	s_and_b64 s[16:17], s[18:19], s[16:17]
	v_cmp_gt_i32_e64 s[12:13], 42, v146
	s_and_b64 s[14:15], s[16:17], s[14:15]
	v_cmp_gt_i32_e64 s[10:11], 41, v146
	s_and_b64 s[12:13], s[14:15], s[12:13]
	v_cmp_gt_i32_e64 s[8:9], 40, v146
	s_and_b64 s[10:11], s[12:13], s[10:11]
	v_cmp_gt_i32_e64 s[6:7], 35, v146
	s_and_b64 s[8:9], s[10:11], s[8:9]
	v_cmp_gt_i32_e64 s[4:5], 34, v146
	s_and_b64 s[6:7], s[8:9], s[6:7]
	v_cmp_gt_i32_e64 s[2:3], 33, v146
	s_and_b64 s[4:5], s[6:7], s[4:5]
	v_cmp_gt_i32_e32 vcc, 32, v146
	s_and_b64 s[2:3], s[4:5], s[2:3]
	v_cndmask_b32_e64 v81, v81, v243, s[62:63]
	s_mov_b32 s62, 0x41200000
	v_cndmask_b32_e64 v80, v80, v243, s[60:61]
	s_mov_b32 s60, 2.0
	v_cndmask_b32_e64 v79, v79, v243, s[58:59]
	s_mov_b32 s58, 0x41800000
	s_and_b64 vcc, s[2:3], vcc
	s_mov_b32 s63, 0x41300000
	s_mov_b32 s61, 0x40400000
	s_mov_b32 s59, 0x41880000
	v_cndmask_b32_e64 v78, v78, v243, s[56:57]
	v_cndmask_b32_e64 v77, v77, v243, s[54:55]
	v_cndmask_b32_e64 v76, v76, v243, s[52:53]
	v_cndmask_b32_e64 v75, v75, v243, s[50:51]
	v_cndmask_b32_e64 v74, v74, v243, s[48:49]
	v_cndmask_b32_e64 v73, v73, v243, s[46:47]
	v_cndmask_b32_e64 v72, v72, v243, s[44:45]
	v_cndmask_b32_e64 v71, v71, v243, s[42:43]
	v_cndmask_b32_e64 v70, v70, v243, s[40:41]
	v_cndmask_b32_e64 v69, v69, v243, s[38:39]
	v_cndmask_b32_e64 v68, v68, v243, s[36:37]
	v_cndmask_b32_e64 v67, v67, v243, s[34:35]
	v_cndmask_b32_e64 v97, v97, v243, s[30:31]
	v_cndmask_b32_e64 v96, v96, v243, s[28:29]
	v_cndmask_b32_e64 v95, v95, v243, s[26:27]
	v_cndmask_b32_e64 v94, v94, v243, s[24:25]
	v_cndmask_b32_e64 v93, v93, v243, s[22:23]
	v_cndmask_b32_e64 v92, v92, v243, s[20:21]
	v_cndmask_b32_e64 v91, v91, v243, s[18:19]
	v_cndmask_b32_e64 v90, v90, v243, s[16:17]
	v_cndmask_b32_e64 v89, v89, v243, s[14:15]
	v_cndmask_b32_e64 v88, v88, v243, s[12:13]
	v_cndmask_b32_e64 v87, v87, v243, s[10:11]
	v_cndmask_b32_e64 v86, v86, v243, s[8:9]
	v_cndmask_b32_e64 v85, v85, v243, s[6:7]
	v_cndmask_b32_e64 v84, v84, v243, s[4:5]
	v_cndmask_b32_e64 v83, v83, v243, s[2:3]
	v_cndmask_b32_e32 v82, v82, v243, vcc

.LBB0_1266:
	v_cndmask_b32_e64 v176, v146, v200, s[2:3]
	s_waitcnt lgkmcnt(0)
	s_barrier
	v_mul_f32_e32 v150, 0xbe0293ee, v176
	v_fmamk_f32 v66, v66, 0x3e0293ee, v150
	v_fmamk_f32 v67, v67, 0x3e0293ee, v150
	v_fmamk_f32 v68, v68, 0x3e0293ee, v150
	v_fmamk_f32 v69, v69, 0x3e0293ee, v150
	v_fmamk_f32 v70, v70, 0x3e0293ee, v150
	v_fmamk_f32 v71, v71, 0x3e0293ee, v150
	v_fmamk_f32 v72, v72, 0x3e0293ee, v150
	v_fmamk_f32 v73, v73, 0x3e0293ee, v150
	v_fmamk_f32 v74, v74, 0x3e0293ee, v150
	v_fmamk_f32 v75, v75, 0x3e0293ee, v150
	v_fmamk_f32 v76, v76, 0x3e0293ee, v150
	v_fmamk_f32 v77, v77, 0x3e0293ee, v150
	v_fmamk_f32 v78, v78, 0x3e0293ee, v150
	v_fmamk_f32 v79, v79, 0x3e0293ee, v150
	v_fmamk_f32 v80, v80, 0x3e0293ee, v150
	v_fmamk_f32 v81, v81, 0x3e0293ee, v150
	v_fmamk_f32 v151, v82, 0x3e0293ee, v150
	v_fmamk_f32 v152, v83, 0x3e0293ee, v150
	v_fmamk_f32 v153, v84, 0x3e0293ee, v150
	v_fmamk_f32 v154, v85, 0x3e0293ee, v150
	v_fmamk_f32 v155, v86, 0x3e0293ee, v150
	v_fmamk_f32 v156, v87, 0x3e0293ee, v150
	v_fmamk_f32 v157, v88, 0x3e0293ee, v150
	v_fmamk_f32 v158, v89, 0x3e0293ee, v150
	v_fmamk_f32 v159, v90, 0x3e0293ee, v150
	v_fmamk_f32 v160, v91, 0x3e0293ee, v150
	v_fmamk_f32 v161, v92, 0x3e0293ee, v150
	v_fmamk_f32 v178, v93, 0x3e0293ee, v150
	v_fmamk_f32 v179, v94, 0x3e0293ee, v150
	v_fmamk_f32 v200, v95, 0x3e0293ee, v150
	v_fmamk_f32 v206, v96, 0x3e0293ee, v150
	v_fmac_f32_e32 v150, 0x3e0293ee, v97
	v_exp_f32_e32 v208, v66
	v_exp_f32_e32 v209, v67
	v_exp_f32_e32 v210, v68
	v_exp_f32_e32 v211, v69
	v_exp_f32_e32 v212, v70
	v_exp_f32_e32 v213, v71
	v_exp_f32_e32 v214, v72
	v_exp_f32_e32 v215, v73
	v_exp_f32_e32 v216, v74
	v_exp_f32_e32 v217, v75
	v_exp_f32_e32 v218, v76
	v_exp_f32_e32 v219, v77
	v_exp_f32_e32 v220, v78
	v_exp_f32_e32 v221, v79
	v_exp_f32_e32 v222, v80
	v_exp_f32_e32 v223, v81
	s_add_i32 s2, s85, 1
	v_cvt_f32_i32_e32 v66, v199
	s_lshr_b32 s2, s2, 8
	v_lshrrev_b32_sdwa v67, s2, v192 dst_sel:DWORD dst_unused:UNUSED_PAD src0_sel:DWORD src1_sel:WORD_0
	v_and_b32_e32 v67, 1, v67
	v_mul_f32_e64 v66, -v162, v66
	v_cmp_eq_u32_e32 vcc, 1, v67
	s_mov_b32 s2, 0x41900000
	s_mov_b32 s3, 0x41980000
	v_cndmask_b32_e32 v82, v243, v66, vcc
	v_pk_fma_f32 v[76:77], v[170:171], s[2:3], v[82:83] op_sel_hi:[1,1,0]
	s_mov_b32 s2, 0x41c00000
	s_mov_b32 s3, 0x41c80000
	v_pk_fma_f32 v[78:79], v[170:171], s[2:3], v[82:83] op_sel_hi:[1,1,0]
	s_mov_b32 s2, 0x41d00000
	s_mov_b32 s3, 0x41d80000
	v_pk_fma_f32 v[80:81], v[170:171], s[2:3], v[82:83] op_sel_hi:[1,1,0]
	s_mov_b32 s2, 0x42000000
	v_mov_b32_e32 v163, v162
	s_mov_b32 s3, 0x42040000
	v_fma_f32 v66, 0, v162, v82
	v_add_f32_e32 v67, v162, v82
	v_pk_fma_f32 v[68:69], v[170:171], s[60:61], v[82:83] op_sel_hi:[1,1,0]
	v_pk_fma_f32 v[70:71], v[170:171], s[74:75], v[82:83] op_sel_hi:[1,1,0]
	v_pk_fma_f32 v[72:73], v[170:171], s[62:63], v[82:83] op_sel_hi:[1,1,0]
	v_pk_fma_f32 v[74:75], v[170:171], s[58:59], v[82:83] op_sel_hi:[1,1,0]
	v_pk_fma_f32 v[96:97], v[162:163], s[68:69], v[82:83] op_sel_hi:[1,1,0]
	v_pk_fma_f32 v[94:95], v[162:163], s[96:97], v[82:83] op_sel_hi:[1,1,0]
	v_pk_fma_f32 v[92:93], v[162:163], s[94:95], v[82:83] op_sel_hi:[1,1,0]
	v_pk_fma_f32 v[90:91], v[162:163], s[92:93], v[82:83] op_sel_hi:[1,1,0]
	v_pk_fma_f32 v[88:89], v[162:163], s[90:91], v[82:83] op_sel_hi:[1,1,0]
	v_pk_fma_f32 v[86:87], v[162:163], s[88:89], v[82:83] op_sel_hi:[1,1,0]
	v_pk_fma_f32 v[84:85], v[162:163], s[86:87], v[82:83] op_sel_hi:[1,1,0]
	v_pk_fma_f32 v[82:83], v[168:169], s[2:3], v[82:83] op_sel_hi:[1,1,0]
	s_setprio 1
	ds_read_b128 v[146:149], v195 offset:32768
	ds_read_b128 v[224:227], v195 offset:40960
	s_waitcnt lgkmcnt(1)
	v_mfma_f32_32x32x16_bf16 v[66:81], v[146:149], v[126:129], v[66:81]
	ds_read_b128 v[146:149], v196 offset:32768
	s_waitcnt lgkmcnt(1)
	v_mfma_f32_32x32x16_bf16 v[82:97], v[224:227], v[126:129], v[82:97]
	ds_read_b128 v[224:227], v196 offset:40960
	s_waitcnt lgkmcnt(1)
	v_mfma_f32_32x32x16_bf16 v[66:81], v[146:149], v[122:125], v[66:81]
	ds_read_b128 v[146:149], v197 offset:32768
	s_waitcnt lgkmcnt(1)
	v_mfma_f32_32x32x16_bf16 v[82:97], v[224:227], v[122:125], v[82:97]
	ds_read_b128 v[224:227], v197 offset:40960
	s_waitcnt lgkmcnt(1)
	v_mfma_f32_32x32x16_bf16 v[66:81], v[146:149], v[118:121], v[66:81]
	ds_read_b128 v[146:149], v198 offset:32768
	s_waitcnt lgkmcnt(1)
	v_mfma_f32_32x32x16_bf16 v[82:97], v[224:227], v[118:121], v[82:97]
	ds_read_b128 v[224:227], v198 offset:40960
	s_waitcnt lgkmcnt(1)
	v_mfma_f32_32x32x16_bf16 v[66:81], v[146:149], v[114:117], v[66:81]
	ds_read_b128 v[146:149], v195 offset:32896
	s_waitcnt lgkmcnt(1)
	v_mfma_f32_32x32x16_bf16 v[82:97], v[224:227], v[114:117], v[82:97]
	ds_read_b128 v[224:227], v195 offset:41088
	s_waitcnt lgkmcnt(1)
	v_mfma_f32_32x32x16_bf16 v[66:81], v[146:149], v[110:113], v[66:81]
	ds_read_b128 v[146:149], v196 offset:32896
	s_waitcnt lgkmcnt(1)
	v_mfma_f32_32x32x16_bf16 v[82:97], v[224:227], v[110:113], v[82:97]
	ds_read_b128 v[224:227], v196 offset:41088
	s_waitcnt lgkmcnt(1)
	v_mfma_f32_32x32x16_bf16 v[66:81], v[146:149], v[106:109], v[66:81]
	ds_read_b128 v[146:149], v197 offset:32896
	s_waitcnt lgkmcnt(1)
	v_mfma_f32_32x32x16_bf16 v[82:97], v[224:227], v[106:109], v[82:97]
	ds_read_b128 v[224:227], v197 offset:41088
	s_waitcnt lgkmcnt(1)
	v_mfma_f32_32x32x16_bf16 v[66:81], v[146:149], v[102:105], v[66:81]
	ds_read_b128 v[146:149], v198 offset:32896
	s_waitcnt lgkmcnt(1)
	v_mfma_f32_32x32x16_bf16 v[82:97], v[224:227], v[102:105], v[82:97]
	ds_read_b128 v[224:227], v198 offset:41088
	s_waitcnt lgkmcnt(1)
	v_mfma_f32_32x32x16_bf16 v[66:81], v[146:149], v[98:101], v[66:81]
	s_waitcnt lgkmcnt(0)
	v_mfma_f32_32x32x16_bf16 v[82:97], v[224:227], v[98:101], v[82:97]
	s_setprio 0
	v_add_f32_e32 v146, 0, v208
	v_add_f32_e32 v146, v209, v146
	v_add_f32_e32 v146, v210, v146
	v_add_f32_e32 v146, v211, v146
	v_add_f32_e32 v146, v212, v146
	v_add_f32_e32 v146, v213, v146
	v_add_f32_e32 v146, v214, v146
	v_add_f32_e32 v146, v215, v146
	v_add_f32_e32 v146, v216, v146
	v_add_f32_e32 v146, v217, v146
	v_add_f32_e32 v146, v218, v146
	v_add_f32_e32 v146, v219, v146
	v_exp_f32_e32 v225, v151
	v_add_f32_e32 v146, v220, v146
	v_exp_f32_e32 v226, v152
	v_add_f32_e32 v146, v221, v146
	v_exp_f32_e32 v227, v153
	v_add_f32_e32 v146, v222, v146
	v_exp_f32_e32 v228, v154
	v_add_f32_e32 v146, v223, v146
	v_exp_f32_e32 v229, v155
	v_add_f32_e32 v146, v225, v146
	v_exp_f32_e32 v156, v156
	v_add_f32_e32 v146, v226, v146
	v_exp_f32_e32 v157, v157
	v_add_f32_e32 v146, v227, v146
	v_exp_f32_e32 v158, v158
	v_add_f32_e32 v146, v228, v146
	v_exp_f32_e32 v159, v159
	v_add_f32_e32 v146, v229, v146
	v_exp_f32_e32 v160, v160
	v_add_f32_e32 v146, v156, v146
	v_exp_f32_e32 v161, v161
	v_add_f32_e32 v146, v157, v146
	v_exp_f32_e32 v178, v178
	v_add_f32_e32 v146, v158, v146
	v_exp_f32_e32 v179, v179
	v_add_f32_e32 v146, v159, v146
	v_exp_f32_e32 v200, v200
	v_add_f32_e32 v146, v160, v146
	v_exp_f32_e32 v206, v206
	v_add_f32_e32 v146, v161, v146
	v_exp_f32_e32 v230, v150
	v_add_f32_e32 v146, v178, v146
	v_add_f32_e32 v146, v179, v146
	v_add_f32_e32 v146, v200, v146
	v_add_f32_e32 v146, v206, v146
	v_add_f32_e32 v163, v230, v146
	v_mov_b32_e32 v224, v163
	v_cvt_pk_bf16_f32 v146, v208, v209
	v_cvt_pk_bf16_f32 v147, v210, v211
	v_cvt_pk_bf16_f32 v148, v212, v213
	v_cvt_pk_bf16_f32 v149, v214, v215
	v_cvt_pk_bf16_f32 v150, v216, v217
	v_cvt_pk_bf16_f32 v151, v218, v219
	v_cvt_pk_bf16_f32 v152, v220, v221
	v_cvt_pk_bf16_f32 v153, v222, v223
	v_cvt_pk_bf16_f32 v154, v225, v226
	v_cvt_pk_bf16_f32 v155, v227, v228
	v_cvt_pk_bf16_f32 v156, v229, v156
	v_cvt_pk_bf16_f32 v157, v157, v158
	v_cvt_pk_bf16_f32 v158, v159, v160
	v_cvt_pk_bf16_f32 v159, v161, v178
	v_cvt_pk_bf16_f32 v160, v179, v200
	v_cvt_pk_bf16_f32 v161, v206, v230
	s_nop 1
	v_permlane32_swap_b32_e32 v163, v224
	v_permlane32_swap_b32_e32 v146, v148
	v_permlane32_swap_b32_e32 v147, v149
	v_permlane32_swap_b32_e32 v150, v152
	v_permlane32_swap_b32_e32 v151, v153
	v_permlane32_swap_b32_e32 v154, v156
	v_permlane32_swap_b32_e32 v155, v157
	v_permlane32_swap_b32_e32 v158, v160
	v_permlane32_swap_b32_e32 v159, v161
	s_add_i32 s2, s84, 1
	s_cmp_lt_u32 s2, s83
	s_cselect_b64 s[76:77], -1, 0
	s_cmp_ge_u32 s2, s83
	s_cbranch_scc1 .LBB0_1268
	v_add_u32_e32 v138, 0x41, v177
	v_add_u32_e32 v140, 0x61, v177
	v_mad_i64_i32 v[130:131], s[2:3], v138, s71, v[172:173]
	v_mad_i64_i32 v[134:135], s[2:3], v140, s71, v[172:173]
	v_mad_i64_i32 v[138:139], s[2:3], v138, s71, v[174:175]
	v_mad_i64_i32 v[142:143], s[2:3], v140, s71, v[174:175]
	global_load_dwordx4 v[130:133], v[130:131], off
	s_nop 0
	global_load_dwordx4 v[134:137], v[134:135], off
	s_nop 0
	global_load_dwordx4 v[138:141], v[138:139], off
	s_nop 0
	global_load_dwordx4 v[142:145], v[142:143], off
